# baseline (speedup 1.0000x reference)
_Z11gram_kernelPKfPKiS0_S0_S0_S0_S0_S0_S0_S0_S0_Pf:
	s_load_dwordx4 s[24:27], s[0:1], 0x0
	s_load_dwordx2 s[28:29], s[0:1], 0x40
	s_load_dwordx4 s[20:23], s[0:1], 0x30
	s_load_dwordx2 s[10:11], s[0:1], 0x58
	s_load_dwordx2 s[44:45], s[0:1], 0x20
	s_load_dwordx2 s[68:69], s[0:1], 0x10
	s_ashr_i32 s30, s2, 1
	v_mov_b32_e32 v11, 0
	s_ashr_i32 s31, s30, 31
	s_lshl_b32 s46, s30, 11
	s_lshl_b32 s3, s2, 10
	s_ashr_i32 s47, s46, 31
	s_and_b32 s33, s3, 0x400
	v_lshlrev_b32_e32 v46, 2, v0
	v_mov_b32_e32 v47, 0
	v_lshlrev_b32_e32 v212, 1, v0
	v_mov_b32_e32 v213, v47
	v_lshrrev_b32_e32 v219, 6, v0
	v_bfe_u32 v214, v0, 5, 1
	v_and_b32_e32 v220, 31, v0
	s_or_b32 s3, s46, s33
	v_lshlrev_b32_e32 v216, 4, v219
	v_lshlrev_b32_e32 v221, 3, v214
	v_or3_b32 v1, s3, v216, v221
	v_lshlrev_b32_e32 v232, 4, v220
	v_and_b32_e32 v218, 63, v0
	s_mov_b32 s39, 0x20000
	s_brev_b32 s38, 16
	v_lshl_or_b32 v180, v1, 9, v232
	v_add_u32_e32 v1, 0x10000, v180
	s_lshl_b64 s[4:5], s[46:47], 2
	s_lshl_b32 s3, s33, 2
	s_waitcnt lgkmcnt(0)
	s_mov_b64 s[36:37], s[24:25]
	s_and_b32 s37, s37, 0xffff
	s_add_u32 s26, s26, s4
	s_addc_u32 s27, s27, s5
	s_add_u32 s26, s26, s3
	s_addc_u32 s27, s27, 0
	v_lshl_add_u64 v[32:33], v[212:213], 2, s[26:27]
	global_load_dwordx2 v[32:33], v[32:33], off
	buffer_load_dwordx4 v[34:37], v180, s[36:39], 0 offen nt
	buffer_load_dwordx4 v[38:41], v180, s[36:39], 0 offen offset:512 nt
	buffer_load_dwordx4 v[42:45], v180, s[36:39], 0 offen offset:1024 nt
	buffer_load_dwordx4 v[96:99], v180, s[36:39], 0 offen offset:1536 nt
	buffer_load_dwordx4 v[100:103], v180, s[36:39], 0 offen offset:2048 nt
	buffer_load_dwordx4 v[104:107], v180, s[36:39], 0 offen offset:2560 nt
	buffer_load_dwordx4 v[108:111], v180, s[36:39], 0 offen offset:3072 nt
	buffer_load_dwordx4 v[112:115], v180, s[36:39], 0 offen offset:3584 nt
	buffer_load_dwordx4 v[116:119], v1, s[36:39], 0 offen nt
	buffer_load_dwordx4 v[120:123], v1, s[36:39], 0 offen offset:512 nt
	buffer_load_dwordx4 v[124:127], v1, s[36:39], 0 offen offset:1024 nt
	buffer_load_dwordx4 v[128:131], v1, s[36:39], 0 offen offset:1536 nt
	buffer_load_dwordx4 v[132:135], v1, s[36:39], 0 offen offset:2048 nt
	buffer_load_dwordx4 v[136:139], v1, s[36:39], 0 offen offset:2560 nt
	buffer_load_dwordx4 v[140:143], v1, s[36:39], 0 offen offset:3072 nt
	buffer_load_dwordx4 v[144:147], v1, s[36:39], 0 offen offset:3584 nt
	s_lshl_b64 s[4:5], s[30:31], 14
	s_add_u32 s48, s20, s4
	s_addc_u32 s49, s21, s5
	s_movk_i32 s3, 0x160
	v_cmp_gt_u32_e32 vcc, s3, v0
	s_mov_b32 s3, 0x10000
	v_lshrrev_b32_e32 v227, 5, v0
	v_and_b32_e32 v228, 0x7c, v46
	v_add_u32_e32 v2, 0x200, v0
	v_lshrrev_b32_e32 v229, 5, v2
	v_mul_u32_u24_e32 v246, 0x110, v227
	v_lshl_add_u32 v246, v220, 3, v246
	v_add_u32_e32 v246, 0x10000, v246
	v_lshlrev_b32_e32 v247, 2, v46
	s_waitcnt vmcnt(16)
	v_cmp_ne_u32_e64 s[6:7], 0, v32
	v_cmp_ne_u32_e64 s[4:5], 0, v33
	v_cmp_eq_u32_e64 s[8:9], 0, v218
	s_nop 0
	s_and_saveexec_b64 s[12:13], s[8:9]
	s_cbranch_execz .LBB0_6
	s_bcnt1_i32_b64 s6, s[6:7]
	s_bcnt1_i32_b64 s4, s[4:5]
	v_mov_b32_e32 v1, 0x21100
	s_add_i32 s4, s4, s6
	v_lshl_add_u32 v1, v219, 2, v1
	v_mov_b32_e32 v2, s4
	ds_write_b32 v1, v2
